# GQA attention fast softmax behind a run-time bound check on the q/k gains (original code kept as fallback); K fragments two rounds ahead
# baseline (speedup 1.0000x reference)
.LBB0_871:
	v_writelane_b32 v252, s96, 34
	s_mov_b64 s[90:91], s[92:93]
	s_andn2_b64 vcc, exec, s[86:87]
	v_writelane_b32 v252, s97, 35
	s_nop 0
	v_readlane_b32 s29, v252, 17
	s_cbranch_vccnz .LBB0_889
	v_cvt_f32_ubyte0_e32 v0, s89
	v_rcp_iflag_f32_e32 v0, v0
	s_and_b64 s[2:3], s[0:1], exec
	s_cselect_b32 s2, 0x200, 0
	s_add_u32 s58, s82, s2
	s_mul_i32 s72, s62, s29
	v_mul_f32_e32 v0, 0x4f7ffffe, v0
	s_addc_u32 s59, s83, 0
	s_lshl_b64 s[92:93], s[72:73], 1
	v_cvt_u32_f32_e32 v0, v0
	s_add_u32 s21, s66, s92
	s_addc_u32 s22, s67, s93
	s_add_u32 s23, s85, s92
	s_addc_u32 s24, s81, s93
	s_sub_i32 s2, 0, s89
	v_readfirstlane_b32 s3, v0
	s_mul_i32 s2, s2, s3
	s_mov_b32 s63, s73
	s_mul_hi_u32 s2, s3, s2
	s_lshl_b64 s[96:97], s[62:63], 7
	s_add_i32 s25, s3, s2
	s_lshl_b32 s38, s62, 5
	s_mul_i32 s3, s62, 0x180
	s_mul_hi_u32 s2, s62, 0x180
	s_add_u32 s6, s10, s3
	s_addc_u32 s7, s11, s2
	s_add_u32 s64, s64, s6
	s_addc_u32 s65, s65, s7
	s_lshl_b64 s[6:7], s[62:63], 8
	s_add_u32 s66, s66, s3
	s_mov_b32 s20, 0
	s_addc_u32 s67, s67, s2
	s_mov_b32 s3, s94
	v_readlane_b32 s8, v255, 34
	v_readlane_b32 s9, v255, 35
	s_nop 4
	s_load_dwordx2 s[8:9], s[8:9], 0x50
	s_and_b64 s[10:11], s[0:1], exec
	s_cselect_b32 s10, 0x200, 0
	v_mbcnt_lo_u32_b32 v0, -1, 0
	v_mbcnt_hi_u32_b32 v0, -1, v0
	v_lshlrev_b32_e32 v0, 3, v0
	s_waitcnt lgkmcnt(0)
	s_add_u32 s8, s8, s10
	s_addc_u32 s9, s9, 0
	global_load_dwordx2 v[2:3], v0, s[58:59]
	global_load_dwordx2 v[4:5], v0, s[8:9]
	s_waitcnt vmcnt(0)
	v_max_f32_e64 v2, |v2|, |v3|
	v_max_f32_e64 v4, |v4|, |v5|
	s_nop 1
	v_max_f32_dpp v2, v2, v2 quad_perm:[1,0,3,2] row_mask:0xf bank_mask:0xf
	v_max_f32_dpp v4, v4, v4 quad_perm:[1,0,3,2] row_mask:0xf bank_mask:0xf
	s_nop 1
	v_max_f32_dpp v2, v2, v2 quad_perm:[2,3,0,1] row_mask:0xf bank_mask:0xf
	v_max_f32_dpp v4, v4, v4 quad_perm:[2,3,0,1] row_mask:0xf bank_mask:0xf
	s_nop 1
	v_max_f32_dpp v2, v2, v2 row_half_mirror row_mask:0xf bank_mask:0xf
	v_max_f32_dpp v4, v4, v4 row_half_mirror row_mask:0xf bank_mask:0xf
	s_nop 1
	v_max_f32_dpp v2, v2, v2 row_mirror row_mask:0xf bank_mask:0xf
	v_max_f32_dpp v4, v4, v4 row_mirror row_mask:0xf bank_mask:0xf
	s_nop 1
	v_readlane_b32 s8, v2, 0
	v_readlane_b32 s9, v2, 16
	v_readlane_b32 s10, v2, 32
	v_readlane_b32 s11, v2, 48
	v_readlane_b32 s12, v4, 0
	v_readlane_b32 s13, v4, 16
	v_readlane_b32 s14, v4, 32
	v_readlane_b32 s15, v4, 48
	s_max_u32 s8, s8, s9
	s_max_u32 s10, s10, s11
	s_max_u32 s12, s12, s13
	s_max_u32 s14, s14, s15
	s_max_u32 s8, s8, s10
	s_max_u32 s12, s12, s14
	v_mov_b32_e32 v2, s8
	v_mul_f32_e32 v2, s12, v2
	s_nop 1
	v_readfirstlane_b32 s8, v2
	s_cmp_lt_u32 s8, 0x407ae148
	s_cbranch_scc0 .Lgqa_slow_874
	s_branch .LBB0_874

.LBB0_887:
	ds_read_b128 v[96:99], v216 offset:49152
	ds_read_b128 v[100:103], v216 offset:57344
	s_waitcnt lgkmcnt(1)
	v_mfma_f32_32x32x16_bf16 v[112:127], v[96:99], v[138:141], 0
	s_waitcnt lgkmcnt(0)
	v_mfma_f32_32x32x16_bf16 v[96:111], v[100:103], v[138:141], 0
	ds_read_b128 v[138:141], v218 offset:49152
	s_waitcnt vmcnt(3)
	ds_read_b128 v[162:165], v218 offset:57344
	v_add_f32_e32 v128, v64, v65
	v_add_f32_e32 v128, v66, v128
	s_waitcnt lgkmcnt(1)
	v_mfma_f32_32x32x16_bf16 v[112:127], v[138:141], v[154:157], v[112:127]
	v_add_f32_e32 v128, v67, v128
	v_add_f32_e32 v128, v68, v128
	v_add_f32_e32 v128, v69, v128
	v_add_f32_e32 v128, v70, v128
	v_add_f32_e32 v128, v71, v128
	s_waitcnt lgkmcnt(0)
	v_mfma_f32_32x32x16_bf16 v[96:111], v[162:165], v[154:157], v[96:111]
	ds_read_b128 v[138:141], v219 offset:49152
	ds_read_b128 v[154:157], v219 offset:57344
	s_waitcnt lgkmcnt(1)
	v_mfma_f32_32x32x16_bf16 v[112:127], v[138:141], v[158:161], v[112:127]
	s_waitcnt lgkmcnt(0)
	v_mfma_f32_32x32x16_bf16 v[96:111], v[154:157], v[158:161], v[96:111]
	ds_read_b128 v[138:141], v220 offset:49152
	ds_read_b128 v[154:157], v220 offset:57344
	s_waitcnt lgkmcnt(1)
	v_mfma_f32_32x32x16_bf16 v[112:127], v[138:141], v[150:153], v[112:127]
	s_waitcnt lgkmcnt(0)
	v_mfma_f32_32x32x16_bf16 v[96:111], v[154:157], v[150:153], v[96:111]
	ds_read_b128 v[138:141], v221 offset:49152
	ds_read_b128 v[150:153], v221 offset:57344
	s_waitcnt lgkmcnt(1)
	v_mfma_f32_32x32x16_bf16 v[112:127], v[138:141], v[146:149], v[112:127]
	s_waitcnt lgkmcnt(0)
	v_mfma_f32_32x32x16_bf16 v[96:111], v[150:153], v[146:149], v[96:111]
	ds_read_b128 v[138:141], v222 offset:49152
	ds_read_b128 v[146:149], v222 offset:57344
	s_waitcnt lgkmcnt(1)
	v_mfma_f32_32x32x16_bf16 v[112:127], v[138:141], v[142:145], v[112:127]
	s_waitcnt lgkmcnt(0)
	v_mfma_f32_32x32x16_bf16 v[96:111], v[146:149], v[142:145], v[96:111]
	ds_read_b128 v[138:141], v224 offset:49152
	ds_read_b128 v[142:145], v224 offset:57344
	s_waitcnt lgkmcnt(1)
	v_mfma_f32_32x32x16_bf16 v[112:127], v[138:141], v[134:137], v[112:127]
	s_waitcnt lgkmcnt(0)
	v_mfma_f32_32x32x16_bf16 v[96:111], v[142:145], v[134:137], v[96:111]
	ds_read_b128 v[134:137], v223 offset:49152
	ds_read_b128 v[138:141], v223 offset:57344
	s_waitcnt lgkmcnt(1)
	v_mfma_f32_32x32x16_bf16 v[112:127], v[134:137], v[130:133], v[112:127]
	s_waitcnt lgkmcnt(0)
	v_mfma_f32_32x32x16_bf16 v[96:111], v[138:141], v[130:133], v[96:111]
	v_add_f32_e32 v130, v72, v73
	v_add_f32_e32 v131, v80, v81
	v_add_f32_e32 v132, v194, v195
	v_add_f32_e32 v130, v74, v130
	v_add_f32_e32 v131, v82, v131
	v_add_f32_e32 v132, v196, v132
	v_add_f32_e32 v130, v75, v130
	v_add_f32_e32 v131, v83, v131
	v_add_f32_e32 v132, v197, v132
	v_add_f32_e32 v130, v76, v130
	v_add_f32_e32 v131, v84, v131
	v_add_f32_e32 v132, v92, v132
	v_add_f32_e32 v130, v77, v130
	v_add_f32_e32 v131, v85, v131
	v_add_f32_e32 v132, v93, v132
	v_add_f32_e32 v130, v78, v130
	v_add_f32_e32 v131, v86, v131
	v_add_f32_e32 v132, v94, v132
	v_add_f32_e32 v130, v79, v130
	v_add_f32_e32 v131, v87, v131
	v_add_f32_e32 v132, v95, v132
	v_add_f32_e32 v128, v130, v128
	v_add_f32_e32 v130, v132, v131
	v_add_f32_e32 v142, v128, v130
	v_mov_b32_e32 v143, v142
	v_cvt_pk_bf16_f32 v130, v64, v65
	v_cvt_pk_bf16_f32 v131, v66, v67
	v_cvt_pk_bf16_f32 v132, v68, v69
	v_cvt_pk_bf16_f32 v133, v70, v71
	v_cvt_pk_bf16_f32 v72, v72, v73
	v_cvt_pk_bf16_f32 v73, v74, v75
	v_cvt_pk_bf16_f32 v74, v76, v77
	v_cvt_pk_bf16_f32 v75, v78, v79
	s_nop 1
	v_permlane32_swap_b32_e32 v142, v143
	v_permlane32_swap_b32_e32 v72, v74
	v_permlane32_swap_b32_e32 v73, v75
	v_cvt_pk_bf16_f32 v138, v80, v81
	v_cvt_pk_bf16_f32 v139, v82, v83
	v_cvt_pk_bf16_f32 v140, v84, v85
	v_cvt_pk_bf16_f32 v141, v86, v87
	v_cvt_pk_bf16_f32 v134, v194, v195
	v_cvt_pk_bf16_f32 v135, v196, v197
	v_cvt_pk_bf16_f32 v136, v92, v93
	v_cvt_pk_bf16_f32 v137, v94, v95
	v_permlane32_swap_b32_e32 v130, v132
	v_permlane32_swap_b32_e32 v131, v133
	v_permlane32_swap_b32_e32 v138, v140
	v_permlane32_swap_b32_e32 v139, v141
	v_permlane32_swap_b32_e32 v134, v136
	v_permlane32_swap_b32_e32 v135, v137
	ds_read_b64_tr_b16 v[64:65], v209 offset:0
	ds_read_b64_tr_b16 v[66:67], v209 offset:0x800
	ds_read_b64_tr_b16 v[68:69], v209 offset:0x1000
	ds_read_b64_tr_b16 v[70:71], v209 offset:0x1800
	ds_read_b64_tr_b16 v[76:77], v209 offset:0x2000
	ds_read_b64_tr_b16 v[78:79], v209 offset:0x2800
	ds_read_b64_tr_b16 v[80:81], v209 offset:0x3000
	ds_read_b64_tr_b16 v[82:83], v209 offset:0x3800
	s_waitcnt lgkmcnt(0)
	s_nop 0
	v_mfma_f32_32x32x16_bf16 v[0:15], v[64:67], v[130:133], v[0:15]
	v_mfma_f32_32x32x16_bf16 v[0:15], v[68:71], v[72:75], v[0:15]
	v_mfma_f32_32x32x16_bf16 v[0:15], v[76:79], v[138:141], v[0:15]
	ds_read_b64_tr_b16 v[64:65], v209 offset:0x200
	ds_read_b64_tr_b16 v[66:67], v209 offset:0xa00
	ds_read_b64_tr_b16 v[68:69], v209 offset:0x1200
	v_mfma_f32_32x32x16_bf16 v[0:15], v[80:83], v[134:137], v[0:15]
	ds_read_b64_tr_b16 v[70:71], v209 offset:0x1a00
	ds_read_b64_tr_b16 v[76:77], v209 offset:0x2200
	ds_read_b64_tr_b16 v[78:79], v209 offset:0x2a00
	ds_read_b64_tr_b16 v[80:81], v209 offset:0x3200
	ds_read_b64_tr_b16 v[82:83], v209 offset:0x3a00
	s_waitcnt lgkmcnt(0)
	v_mfma_f32_32x32x16_bf16 v[48:63], v[64:67], v[130:133], v[48:63]
	v_mfma_f32_32x32x16_bf16 v[48:63], v[68:71], v[72:75], v[48:63]
	v_mfma_f32_32x32x16_bf16 v[48:63], v[76:79], v[138:141], v[48:63]
	v_mov_b32_e32 v128, 1.0
	v_mov_b32_e32 v208, 1.0
	ds_read_b64_tr_b16 v[64:65], v209 offset:0x400
	ds_read_b64_tr_b16 v[66:67], v209 offset:0xc00
	ds_read_b64_tr_b16 v[68:69], v209 offset:0x1400
	v_mfma_f32_32x32x16_bf16 v[48:63], v[80:83], v[134:137], v[48:63]
	ds_read_b64_tr_b16 v[70:71], v209 offset:0x1c00
	ds_read_b64_tr_b16 v[76:77], v209 offset:0x2400
	ds_read_b64_tr_b16 v[78:79], v209 offset:0x2c00
	ds_read_b64_tr_b16 v[80:81], v209 offset:0x3400
	ds_read_b64_tr_b16 v[82:83], v209 offset:0x3c00
	s_waitcnt lgkmcnt(0)
	v_mfma_f32_32x32x16_bf16 v[32:47], v[64:67], v[130:133], v[32:47]
	v_mov_b32_e32 v84, v100
	v_mov_b32_e32 v85, v101
	v_mov_b32_e32 v86, v102
	v_mov_b32_e32 v87, v103
	v_mov_b32_e32 v88, v104
	v_mov_b32_e32 v89, v105
	v_mov_b32_e32 v90, v106
	v_mov_b32_e32 v91, v107
	v_exp_f32_e32 v64, v112
	v_exp_f32_e32 v65, v113
	v_exp_f32_e32 v66, v114
	v_mfma_f32_32x32x16_bf16 v[32:47], v[68:71], v[72:75], v[32:47]
	v_exp_f32_e32 v67, v115
	v_exp_f32_e32 v68, v116
	v_exp_f32_e32 v69, v117
	v_exp_f32_e32 v70, v118
	v_exp_f32_e32 v71, v119
	v_mov_b32_e32 v94, v110
	v_mov_b32_e32 v95, v111
	v_mov_b32_e32 v92, v108
	v_mov_b32_e32 v93, v109
	v_mfma_f32_32x32x16_bf16 v[32:47], v[76:79], v[138:141], v[32:47]
	ds_read_b64_tr_b16 v[76:77], v209 offset:0x600
	ds_read_b64_tr_b16 v[78:79], v209 offset:0xe00
	v_mfma_f32_32x32x16_bf16 v[32:47], v[80:83], v[134:137], v[32:47]
	v_mov_b32_e32 v80, v96
	v_mov_b32_e32 v81, v97
	ds_read_b64_tr_b16 v[96:97], v209 offset:0x1600
	v_mov_b32_e32 v82, v98
	v_mov_b32_e32 v83, v99
	ds_read_b64_tr_b16 v[98:99], v209 offset:0x1e00
	ds_read_b64_tr_b16 v[100:101], v209 offset:0x2600
	ds_read_b64_tr_b16 v[102:103], v209 offset:0x2e00
	ds_read_b64_tr_b16 v[104:105], v209 offset:0x3600
	ds_read_b64_tr_b16 v[106:107], v209 offset:0x3e00
	s_waitcnt lgkmcnt(0)
	v_mfma_f32_32x32x16_bf16 v[16:31], v[76:79], v[130:133], v[16:31]
	v_exp_f32_e32 v76, v124
	v_exp_f32_e32 v77, v125
	v_exp_f32_e32 v78, v126
	v_exp_f32_e32 v79, v127
	v_mfma_f32_32x32x16_bf16 v[16:31], v[96:99], v[72:75], v[16:31]
	v_exp_f32_e32 v72, v120
	v_exp_f32_e32 v73, v121
	v_exp_f32_e32 v74, v122
	v_exp_f32_e32 v75, v123
	s_barrier
	v_mfma_f32_32x32x16_bf16 v[16:31], v[100:103], v[138:141], v[16:31]
	v_mfma_f32_32x32x16_bf16 v[16:31], v[104:107], v[134:137], v[16:31]
	s_branch .LBB0_873
	v_pk_mul_f32 v[14:15], v[14:15], v[128:129] op_sel_hi:[1,0]
	v_pk_mul_f32 v[12:13], v[12:13], v[128:129] op_sel_hi:[1,0]
	v_pk_mul_f32 v[10:11], v[10:11], v[128:129] op_sel_hi:[1,0]
	v_pk_mul_f32 v[8:9], v[8:9], v[128:129] op_sel_hi:[1,0]
	v_pk_mul_f32 v[6:7], v[6:7], v[128:129] op_sel_hi:[1,0]
	v_pk_mul_f32 v[4:5], v[4:5], v[128:129] op_sel_hi:[1,0]
	v_pk_mul_f32 v[2:3], v[2:3], v[128:129] op_sel_hi:[1,0]
	v_pk_mul_f32 v[0:1], v[0:1], v[128:129] op_sel_hi:[1,0]
	v_pk_mul_f32 v[62:63], v[62:63], v[128:129] op_sel_hi:[1,0]
	v_pk_mul_f32 v[60:61], v[60:61], v[128:129] op_sel_hi:[1,0]
	v_pk_mul_f32 v[58:59], v[58:59], v[128:129] op_sel_hi:[1,0]
	v_pk_mul_f32 v[56:57], v[56:57], v[128:129] op_sel_hi:[1,0]
	v_pk_mul_f32 v[54:55], v[54:55], v[128:129] op_sel_hi:[1,0]
	v_pk_mul_f32 v[52:53], v[52:53], v[128:129] op_sel_hi:[1,0]
	v_pk_mul_f32 v[50:51], v[50:51], v[128:129] op_sel_hi:[1,0]
	v_pk_mul_f32 v[48:49], v[48:49], v[128:129] op_sel_hi:[1,0]
	v_pk_mul_f32 v[46:47], v[128:129], v[46:47] op_sel_hi:[0,1]
	v_pk_mul_f32 v[44:45], v[128:129], v[44:45] op_sel_hi:[0,1]
	v_pk_mul_f32 v[42:43], v[128:129], v[42:43] op_sel_hi:[0,1]
	v_pk_mul_f32 v[40:41], v[128:129], v[40:41] op_sel_hi:[0,1]
	v_pk_mul_f32 v[38:39], v[128:129], v[38:39] op_sel_hi:[0,1]
	v_pk_mul_f32 v[36:37], v[128:129], v[36:37] op_sel_hi:[0,1]
	v_pk_mul_f32 v[34:35], v[128:129], v[34:35] op_sel_hi:[0,1]
	v_pk_mul_f32 v[32:33], v[128:129], v[32:33] op_sel_hi:[0,1]
	v_pk_mul_f32 v[30:31], v[128:129], v[30:31] op_sel_hi:[0,1]
	v_pk_mul_f32 v[28:29], v[128:129], v[28:29] op_sel_hi:[0,1]
	v_pk_mul_f32 v[26:27], v[128:129], v[26:27] op_sel_hi:[0,1]
	v_pk_mul_f32 v[24:25], v[128:129], v[24:25] op_sel_hi:[0,1]
	v_pk_mul_f32 v[22:23], v[128:129], v[22:23] op_sel_hi:[0,1]
	v_pk_mul_f32 v[20:21], v[128:129], v[20:21] op_sel_hi:[0,1]
	v_pk_mul_f32 v[18:19], v[128:129], v[18:19] op_sel_hi:[0,1]
	v_pk_mul_f32 v[16:17], v[128:129], v[16:17] op_sel_hi:[0,1]
	s_branch .LBB0_873
.Lgqa_slow_873:
	v_exp_f32_e32 v101, v80
	v_exp_f32_e32 v103, v81
	v_exp_f32_e32 v111, v88
	v_exp_f32_e32 v89, v89
	v_exp_f32_e32 v105, v82
	v_exp_f32_e32 v113, v90
	v_exp_f32_e32 v83, v83
	v_exp_f32_e32 v91, v91
	v_exp_f32_e32 v107, v84
	v_exp_f32_e32 v115, v92
	v_mov_b32_e32 v100, v64
	v_mov_b32_e32 v102, v65
	v_mov_b32_e32 v110, v72
	v_mov_b32_e32 v88, v73
	v_exp_f32_e32 v85, v85
	v_exp_f32_e32 v93, v93
	v_pk_add_f32 v[80:81], v[100:101], v[102:103]
	v_pk_add_f32 v[118:119], v[110:111], v[88:89]
	v_mov_b32_e32 v104, v66
	v_mov_b32_e32 v112, v74
	v_exp_f32_e32 v109, v86
	v_exp_f32_e32 v117, v94
	v_pk_add_f32 v[80:81], v[104:105], v[80:81]
	v_pk_add_f32 v[118:119], v[112:113], v[118:119]
	v_mov_b32_e32 v82, v67
	v_mov_b32_e32 v90, v75
	v_exp_f32_e32 v87, v87
	v_exp_f32_e32 v95, v95
	v_pk_add_f32 v[80:81], v[82:83], v[80:81]
	v_pk_add_f32 v[118:119], v[90:91], v[118:119]
	v_mov_b32_e32 v106, v68
	v_mov_b32_e32 v114, v76
	v_pk_add_f32 v[80:81], v[106:107], v[80:81]
	v_pk_add_f32 v[118:119], v[114:115], v[118:119]
	v_mov_b32_e32 v84, v69
	v_mov_b32_e32 v92, v77
	v_pk_add_f32 v[80:81], v[84:85], v[80:81]
	v_pk_add_f32 v[118:119], v[92:93], v[118:119]
	v_mov_b32_e32 v108, v70
	v_mov_b32_e32 v116, v78
	v_pk_add_f32 v[80:81], v[108:109], v[80:81]
	v_pk_add_f32 v[118:119], v[116:117], v[118:119]
	v_mov_b32_e32 v86, v71
	v_mov_b32_e32 v94, v79
	v_pk_add_f32 v[80:81], v[86:87], v[80:81]
	v_pk_add_f32 v[118:119], v[94:95], v[118:119]
	s_lshl_b32 s2, s33, 12
	v_pk_add_f32 v[80:81], v[118:119], v[80:81]
	s_add_u32 s8, s35, s2
	v_pk_add_f32 v[80:81], v[80:81], v[80:81] op_sel:[0,1] op_sel_hi:[1,0]
	s_addc_u32 s9, s36, 0
	s_lshl_b32 s2, s28, 7
	v_mov_b32_e32 v99, v80
	s_ashr_i32 s3, s2, 31
	s_nop 0
	v_permlane32_swap_b32_e32 v80, v99
	s_lshl_b64 s[2:3], s[2:3], 1
	v_mul_f32_e32 v96, v217, v208
	v_add_f32_e32 v98, v142, v143
	v_mov_b32_e32 v97, v80
	s_add_u32 s8, s8, s2
	v_pk_add_f32 v[80:81], v[96:97], v[98:99]
	v_cvt_pk_bf16_f32 v64, v64, v65
	v_cvt_pk_bf16_f32 v65, v66, v67
	v_cvt_pk_bf16_f32 v66, v68, v69
	v_cvt_pk_bf16_f32 v67, v70, v71
	v_cvt_pk_bf16_f32 v68, v72, v73
	v_cvt_pk_bf16_f32 v69, v74, v75
	v_cvt_pk_bf16_f32 v70, v76, v77
	v_cvt_pk_bf16_f32 v71, v78, v79
	v_cvt_pk_bf16_f32 v72, v101, v103
	v_cvt_pk_bf16_f32 v73, v105, v83
	v_cvt_pk_bf16_f32 v74, v107, v85
	v_cvt_pk_bf16_f32 v75, v109, v87
	v_cvt_pk_bf16_f32 v76, v111, v89
	v_cvt_pk_bf16_f32 v77, v113, v91
	v_cvt_pk_bf16_f32 v78, v115, v93
	v_cvt_pk_bf16_f32 v79, v117, v95
	s_addc_u32 s9, s9, s3
	v_fmac_f32_e32 v81, v80, v128
	v_permlane32_swap_b32_e32 v64, v66
	v_permlane32_swap_b32_e32 v65, v67
	v_permlane32_swap_b32_e32 v68, v70
	v_permlane32_swap_b32_e32 v69, v71
	v_permlane32_swap_b32_e32 v72, v74
	v_permlane32_swap_b32_e32 v73, v75
	v_permlane32_swap_b32_e32 v76, v78
	v_permlane32_swap_b32_e32 v77, v79
	ds_read_b64_tr_b16 v[82:83], v211 offset:0
	ds_read_b64_tr_b16 v[84:85], v211 offset:0x800
	ds_read_b64_tr_b16 v[86:87], v211 offset:0x1000
	ds_read_b64_tr_b16 v[88:89], v211 offset:0x1800
	ds_read_b64_tr_b16 v[90:91], v211 offset:0x2000
	ds_read_b64_tr_b16 v[92:93], v211 offset:0x2800
	ds_read_b64_tr_b16 v[94:95], v211 offset:0x3000
	ds_read_b64_tr_b16 v[96:97], v211 offset:0x3800
	s_waitcnt lgkmcnt(0)
	s_nop 0
	v_mfma_f32_32x32x16_bf16 v[0:15], v[82:85], v[64:67], v[0:15]
	ds_read_b64_tr_b16 v[82:83], v211 offset:0x200
	ds_read_b64_tr_b16 v[84:85], v211 offset:0xa00
	v_mfma_f32_32x32x16_bf16 v[0:15], v[86:89], v[68:71], v[0:15]
	ds_read_b64_tr_b16 v[86:87], v211 offset:0x1200
	ds_read_b64_tr_b16 v[88:89], v211 offset:0x1a00
	v_mfma_f32_32x32x16_bf16 v[0:15], v[90:93], v[72:75], v[0:15]
	ds_read_b64_tr_b16 v[90:91], v211 offset:0x2200
	ds_read_b64_tr_b16 v[92:93], v211 offset:0x2a00
	v_mfma_f32_32x32x16_bf16 v[0:15], v[94:97], v[76:79], v[0:15]
	ds_read_b64_tr_b16 v[94:95], v211 offset:0x3200
	ds_read_b64_tr_b16 v[96:97], v211 offset:0x3a00
	s_waitcnt lgkmcnt(0)
	v_mfma_f32_32x32x16_bf16 v[48:63], v[82:85], v[64:67], v[48:63]
	ds_read_b64_tr_b16 v[82:83], v211 offset:0x400
	ds_read_b64_tr_b16 v[84:85], v211 offset:0xc00
	v_mfma_f32_32x32x16_bf16 v[48:63], v[86:89], v[68:71], v[48:63]
	ds_read_b64_tr_b16 v[86:87], v211 offset:0x1400
	ds_read_b64_tr_b16 v[88:89], v211 offset:0x1c00
	v_mfma_f32_32x32x16_bf16 v[48:63], v[90:93], v[72:75], v[48:63]
	ds_read_b64_tr_b16 v[90:91], v211 offset:0x2400
	ds_read_b64_tr_b16 v[92:93], v211 offset:0x2c00
	v_mfma_f32_32x32x16_bf16 v[48:63], v[94:97], v[76:79], v[48:63]
	ds_read_b64_tr_b16 v[94:95], v211 offset:0x3400
	ds_read_b64_tr_b16 v[96:97], v211 offset:0x3c00
	s_waitcnt lgkmcnt(0)
	v_mfma_f32_32x32x16_bf16 v[32:47], v[82:85], v[64:67], v[32:47]
	ds_read_b64_tr_b16 v[82:83], v211 offset:0x600
	ds_read_b64_tr_b16 v[84:85], v211 offset:0xe00
	v_mfma_f32_32x32x16_bf16 v[32:47], v[86:89], v[68:71], v[32:47]
	ds_read_b64_tr_b16 v[86:87], v211 offset:0x1600
	ds_read_b64_tr_b16 v[88:89], v211 offset:0x1e00
	v_mfma_f32_32x32x16_bf16 v[32:47], v[90:93], v[72:75], v[32:47]
	ds_read_b64_tr_b16 v[90:91], v211 offset:0x2600
	ds_read_b64_tr_b16 v[92:93], v211 offset:0x2e00
	v_mfma_f32_32x32x16_bf16 v[32:47], v[94:97], v[76:79], v[32:47]
	ds_read_b64_tr_b16 v[94:95], v211 offset:0x3600
	ds_read_b64_tr_b16 v[96:97], v211 offset:0x3e00
	s_waitcnt lgkmcnt(0)
	v_mfma_f32_32x32x16_bf16 v[16:31], v[82:85], v[64:67], v[16:31]
	v_rcp_f32_e32 v67, v81
	v_mbcnt_lo_u32_b32 v66, -1, 0
	v_mbcnt_hi_u32_b32 v66, -1, v66
	s_add_i32 s20, s20, 1
	v_add_u32_e32 v64, s80, v66
	v_ashrrev_i32_e32 v64, 1, v64
	v_mul_f32_e32 v0, v67, v0
	v_mul_f32_e32 v1, v67, v1
	v_bfi_b32 v64, s84, v64, v66
	v_cvt_pk_bf16_f32 v0, v0, v1
	v_mul_f32_e32 v1, v67, v2
	v_mul_f32_e32 v2, v67, v3
	v_ashrrev_i32_e32 v65, 31, v64
	v_cvt_pk_bf16_f32 v1, v1, v2
	v_mul_f32_e32 v2, v67, v4
	v_mul_f32_e32 v3, v67, v5
	v_lshlrev_b64 v[64:65], 12, v[64:65]
	v_lshrrev_b32_e32 v66, 1, v66
	v_cvt_pk_bf16_f32 v2, v2, v3
	v_mul_f32_e32 v3, v67, v6
	v_lshl_add_u64 v[64:65], s[8:9], 0, v[64:65]
	v_and_b32_e32 v128, 16, v66
	v_mul_f32_e32 v4, v67, v7
	v_cvt_pk_bf16_f32 v3, v3, v4
	v_lshl_add_u64 v[64:65], v[64:65], 0, v[128:129]
	v_permlane32_swap_b32_e32 v0, v2
	v_permlane32_swap_b32_e32 v1, v3
	global_store_dwordx4 v[64:65], v[0:3], off
	v_mul_f32_e32 v4, v67, v15
	v_mfma_f32_32x32x16_bf16 v[16:31], v[86:89], v[68:71], v[16:31]
	v_mul_f32_e32 v0, v67, v8
	v_mul_f32_e32 v1, v67, v9
	v_cvt_pk_bf16_f32 v0, v0, v1
	v_mul_f32_e32 v1, v67, v10
	v_mul_f32_e32 v2, v67, v11
	v_cvt_pk_bf16_f32 v1, v1, v2
	v_mul_f32_e32 v2, v67, v12
	v_mul_f32_e32 v3, v67, v13
	v_cvt_pk_bf16_f32 v2, v2, v3
	v_mul_f32_e32 v3, v67, v14
	v_cvt_pk_bf16_f32 v3, v3, v4
	v_permlane32_swap_b32_e32 v0, v2
	s_nop 0
	v_permlane32_swap_b32_e32 v1, v3
	global_store_dwordx4 v[64:65], v[0:3], off offset:32
	v_mul_f32_e32 v4, v67, v55
	v_mfma_f32_32x32x16_bf16 v[16:31], v[90:93], v[72:75], v[16:31]
	v_mul_f32_e32 v0, v67, v48
	v_mul_f32_e32 v1, v67, v49
	v_cvt_pk_bf16_f32 v0, v0, v1
	v_mul_f32_e32 v1, v67, v50
	v_mul_f32_e32 v2, v67, v51
	v_cvt_pk_bf16_f32 v1, v1, v2
	v_mul_f32_e32 v2, v67, v52
	v_mul_f32_e32 v3, v67, v53
	v_cvt_pk_bf16_f32 v2, v2, v3
	v_mul_f32_e32 v3, v67, v54
	v_cvt_pk_bf16_f32 v3, v3, v4
	v_permlane32_swap_b32_e32 v0, v2
	s_nop 0
	v_permlane32_swap_b32_e32 v1, v3
	global_store_dwordx4 v[64:65], v[0:3], off offset:64
	v_mul_f32_e32 v4, v67, v63
	v_mfma_f32_32x32x16_bf16 v[16:31], v[94:97], v[76:79], v[16:31]
	v_mul_f32_e32 v0, v67, v56
	v_mul_f32_e32 v1, v67, v57
	v_cvt_pk_bf16_f32 v0, v0, v1
	v_mul_f32_e32 v1, v67, v58
	v_mul_f32_e32 v2, v67, v59
	v_cvt_pk_bf16_f32 v1, v1, v2
	v_mul_f32_e32 v2, v67, v60
	v_mul_f32_e32 v3, v67, v61
	v_cvt_pk_bf16_f32 v2, v2, v3
	v_mul_f32_e32 v3, v67, v62
	v_cvt_pk_bf16_f32 v3, v3, v4
	v_permlane32_swap_b32_e32 v0, v2
	s_nop 0
	v_permlane32_swap_b32_e32 v1, v3
	global_store_dwordx4 v[64:65], v[0:3], off offset:96
	v_mul_f32_e32 v4, v67, v39
	s_lshl_b32 s2, s20, 8
	v_mul_f32_e32 v0, v67, v32
	v_mul_f32_e32 v1, v67, v33
	v_cvt_pk_bf16_f32 v0, v0, v1
	v_mul_f32_e32 v1, v67, v34
	v_mul_f32_e32 v2, v67, v35
	v_cvt_pk_bf16_f32 v1, v1, v2
	v_mul_f32_e32 v2, v67, v36
	v_mul_f32_e32 v3, v67, v37
	v_cvt_pk_bf16_f32 v2, v2, v3
	v_mul_f32_e32 v3, v67, v38
	v_cvt_pk_bf16_f32 v3, v3, v4
	v_permlane32_swap_b32_e32 v0, v2
	s_nop 0
	v_permlane32_swap_b32_e32 v1, v3
	global_store_dwordx4 v[64:65], v[0:3], off offset:128
	v_mul_f32_e32 v4, v67, v47
	s_add_i32 s3, s2, s94
	v_mul_f32_e32 v0, v67, v40
	v_mul_f32_e32 v1, v67, v41
	v_cvt_pk_bf16_f32 v0, v0, v1
	v_mul_f32_e32 v1, v67, v42
	v_mul_f32_e32 v2, v67, v43
	v_cvt_pk_bf16_f32 v1, v1, v2
	v_mul_f32_e32 v2, v67, v44
	v_mul_f32_e32 v3, v67, v45
	v_cvt_pk_bf16_f32 v2, v2, v3
	v_mul_f32_e32 v3, v67, v46
	v_cvt_pk_bf16_f32 v3, v3, v4
	v_permlane32_swap_b32_e32 v0, v2
	s_nop 0
	v_permlane32_swap_b32_e32 v1, v3
	global_store_dwordx4 v[64:65], v[0:3], off offset:160
	v_mul_f32_e32 v4, v67, v23
	s_cmp_lt_i32 s3, s37
	v_mul_f32_e32 v0, v67, v16
	v_mul_f32_e32 v1, v67, v17
	v_cvt_pk_bf16_f32 v0, v0, v1
	v_mul_f32_e32 v1, v67, v18
	v_mul_f32_e32 v2, v67, v19
	v_cvt_pk_bf16_f32 v1, v1, v2
	v_mul_f32_e32 v2, v67, v20
	v_mul_f32_e32 v3, v67, v21
	v_cvt_pk_bf16_f32 v2, v2, v3
	v_mul_f32_e32 v3, v67, v22
	v_cvt_pk_bf16_f32 v3, v3, v4
	v_permlane32_swap_b32_e32 v0, v2
	s_nop 0
	v_permlane32_swap_b32_e32 v1, v3
	global_store_dwordx4 v[64:65], v[0:3], off offset:192
	v_mul_f32_e32 v4, v67, v31
	s_movk_i32 s33, 0xffef
	v_mul_f32_e32 v0, v67, v24
	v_mul_f32_e32 v1, v67, v25
	v_cvt_pk_bf16_f32 v0, v0, v1
	v_mul_f32_e32 v1, v67, v26
	v_mul_f32_e32 v2, v67, v27
	v_cvt_pk_bf16_f32 v1, v1, v2
	v_mul_f32_e32 v2, v67, v28
	v_mul_f32_e32 v3, v67, v29
	v_cvt_pk_bf16_f32 v2, v2, v3
	v_mul_f32_e32 v3, v67, v30
	v_cvt_pk_bf16_f32 v3, v3, v4
	v_permlane32_swap_b32_e32 v0, v2
	s_nop 0
	v_permlane32_swap_b32_e32 v1, v3
	global_store_dwordx4 v[64:65], v[0:3], off offset:224
	s_cbranch_scc0 .LBB0_889

.Lgqa_slow_881:
	ds_read_b128 v[96:99], v216 offset:49152
	ds_read_b128 v[100:103], v216 offset:57344
	ds_read_b128 v[178:181], v218 offset:49152
	ds_read_b128 v[182:185], v218 offset:57344
	v_exp_f32_e32 v80, v80
	v_exp_f32_e32 v81, v81
	s_waitcnt lgkmcnt(3)
	v_mfma_f32_32x32x16_bf16 v[112:127], v[96:99], v[138:141], 0
	v_exp_f32_e32 v82, v82
	v_exp_f32_e32 v83, v83
	v_exp_f32_e32 v84, v84
	v_exp_f32_e32 v92, v92
	v_exp_f32_e32 v85, v85
	v_exp_f32_e32 v93, v93
	v_exp_f32_e32 v86, v86
	s_waitcnt lgkmcnt(2)
	v_mfma_f32_32x32x16_bf16 v[96:111], v[100:103], v[138:141], 0
	v_exp_f32_e32 v94, v94
	v_exp_f32_e32 v87, v87
	v_exp_f32_e32 v95, v95
	s_waitcnt lgkmcnt(1)
	v_mfma_f32_32x32x16_bf16 v[112:127], v[178:181], v[154:157], v[112:127]
	s_waitcnt lgkmcnt(0)
	v_mfma_f32_32x32x16_bf16 v[96:111], v[182:185], v[154:157], v[96:111]
	ds_read_b128 v[178:181], v219 offset:49152
	ds_read_b128 v[182:185], v219 offset:57344
	s_waitcnt lgkmcnt(1)
	v_mfma_f32_32x32x16_bf16 v[112:127], v[178:181], v[158:161], v[112:127]
	s_waitcnt lgkmcnt(0)
	v_mfma_f32_32x32x16_bf16 v[96:111], v[182:185], v[158:161], v[96:111]
	ds_read_b128 v[178:181], v220 offset:49152
	ds_read_b128 v[182:185], v220 offset:57344
	s_waitcnt lgkmcnt(1)
	v_mfma_f32_32x32x16_bf16 v[112:127], v[178:181], v[150:153], v[112:127]
	s_waitcnt lgkmcnt(0)
	v_mfma_f32_32x32x16_bf16 v[96:111], v[182:185], v[150:153], v[96:111]
	ds_read_b128 v[178:181], v221 offset:49152
	ds_read_b128 v[182:185], v221 offset:57344
	s_waitcnt lgkmcnt(1)
	v_mfma_f32_32x32x16_bf16 v[112:127], v[178:181], v[146:149], v[112:127]
	s_waitcnt lgkmcnt(0)
	v_mfma_f32_32x32x16_bf16 v[96:111], v[182:185], v[146:149], v[96:111]
	ds_read_b128 v[178:181], v222 offset:49152
	ds_read_b128 v[182:185], v222 offset:57344
	s_waitcnt lgkmcnt(1)
	v_mfma_f32_32x32x16_bf16 v[112:127], v[178:181], v[142:145], v[112:127]
	s_waitcnt lgkmcnt(0)
	v_mfma_f32_32x32x16_bf16 v[96:111], v[182:185], v[142:145], v[96:111]
	ds_read_b128 v[178:181], v224 offset:49152
	ds_read_b128 v[182:185], v224 offset:57344
	s_waitcnt lgkmcnt(1)
	v_mfma_f32_32x32x16_bf16 v[112:127], v[178:181], v[134:137], v[112:127]
	s_waitcnt lgkmcnt(0)
	v_mfma_f32_32x32x16_bf16 v[96:111], v[182:185], v[134:137], v[96:111]
	ds_read_b128 v[178:181], v223 offset:49152
	ds_read_b128 v[182:185], v223 offset:57344
	s_waitcnt lgkmcnt(1)
	v_mfma_f32_32x32x16_bf16 v[112:127], v[178:181], v[130:133], v[112:127]
	v_exp_f32_e32 v178, v88
	v_exp_f32_e32 v179, v89
	v_exp_f32_e32 v180, v90
	v_exp_f32_e32 v181, v91
	v_add_f32_e32 v88, v64, v65
	v_add_f32_e32 v89, v72, v73
	v_add_f32_e32 v90, v80, v81
	v_add_f32_e32 v91, v178, v179
	v_add_f32_e32 v88, v66, v88
	v_add_f32_e32 v89, v74, v89
	v_add_f32_e32 v90, v82, v90
	v_add_f32_e32 v91, v180, v91
	v_add_f32_e32 v88, v67, v88
	v_add_f32_e32 v89, v75, v89
	v_add_f32_e32 v90, v83, v90
	v_add_f32_e32 v91, v181, v91
	v_add_f32_e32 v88, v68, v88
	v_add_f32_e32 v89, v76, v89
	v_add_f32_e32 v90, v84, v90
	v_add_f32_e32 v91, v92, v91
	v_add_f32_e32 v88, v69, v88
	v_add_f32_e32 v89, v77, v89
	v_add_f32_e32 v90, v85, v90
	v_add_f32_e32 v91, v93, v91
	v_add_f32_e32 v88, v70, v88
	v_add_f32_e32 v89, v78, v89
	v_add_f32_e32 v90, v86, v90
	v_add_f32_e32 v91, v94, v91
	v_add_f32_e32 v88, v71, v88
	v_add_f32_e32 v89, v79, v89
	v_add_f32_e32 v90, v87, v90
	v_add_f32_e32 v91, v95, v91
	v_add_f32_e32 v88, v89, v88
	v_add_f32_e32 v89, v91, v90
	v_add_f32_e32 v227, v88, v89
	v_mov_b32_e32 v228, v227
	v_cvt_pk_bf16_f32 v88, v64, v65
	v_cvt_pk_bf16_f32 v89, v66, v67
	v_cvt_pk_bf16_f32 v90, v68, v69
	v_cvt_pk_bf16_f32 v91, v70, v71
	s_nop 1
	v_permlane32_swap_b32_e32 v227, v228
	v_permlane32_swap_b32_e32 v88, v90
	v_permlane32_swap_b32_e32 v89, v91
	v_cvt_pk_bf16_f32 v72, v72, v73
	v_cvt_pk_bf16_f32 v73, v74, v75
	v_cvt_pk_bf16_f32 v74, v76, v77
	v_cvt_pk_bf16_f32 v75, v78, v79
	v_cvt_pk_bf16_f32 v64, v80, v81
	v_cvt_pk_bf16_f32 v65, v82, v83
	v_cvt_pk_bf16_f32 v66, v84, v85
	v_cvt_pk_bf16_f32 v67, v86, v87
	v_cvt_pk_bf16_f32 v68, v178, v179
	v_cvt_pk_bf16_f32 v69, v180, v181
	v_cvt_pk_bf16_f32 v70, v92, v93
	v_cvt_pk_bf16_f32 v71, v94, v95
	s_waitcnt lgkmcnt(0)
	v_mfma_f32_32x32x16_bf16 v[96:111], v[182:185], v[130:133], v[96:111]
	v_permlane32_swap_b32_e32 v72, v74
	v_permlane32_swap_b32_e32 v73, v75
	v_permlane32_swap_b32_e32 v64, v66
	v_permlane32_swap_b32_e32 v65, v67
	v_permlane32_swap_b32_e32 v68, v70
	v_permlane32_swap_b32_e32 v69, v71
	v_lshl_add_u64 v[76:77], v[200:201], 0, s[92:93]
	global_load_dwordx4 v[178:181], v[76:77], off
	v_lshl_add_u64 v[76:77], v[202:203], 0, s[92:93]
	global_load_dwordx4 v[182:185], v[76:77], off
	v_lshl_add_u64 v[76:77], v[204:205], 0, s[92:93]
	global_load_dwordx4 v[186:189], v[76:77], off
	v_lshl_add_u64 v[76:77], v[206:207], 0, s[92:93]
	global_load_dwordx4 v[190:193], v[76:77], off
	ds_read_b64_tr_b16 v[76:77], v209 offset:0
	ds_read_b64_tr_b16 v[78:79], v209 offset:0x800
	ds_read_b64_tr_b16 v[80:81], v209 offset:0x1000
	ds_read_b64_tr_b16 v[82:83], v209 offset:0x1800
	ds_read_b64_tr_b16 v[84:85], v209 offset:0x2000
	ds_read_b64_tr_b16 v[86:87], v209 offset:0x2800
	ds_read_b64_tr_b16 v[92:93], v209 offset:0x3000
	ds_read_b64_tr_b16 v[94:95], v209 offset:0x3800
	s_waitcnt lgkmcnt(0)
	s_nop 0
	v_mfma_f32_32x32x16_bf16 v[0:15], v[76:79], v[88:91], v[0:15]
	v_max_f32_e32 v76, v97, v97
	v_max_f32_e32 v77, v96, v96
	v_max_f32_e32 v76, v77, v76
	v_max3_f32 v77, v112, v113, v114
	v_max3_f32 v76, v76, v98, v99
	v_max3_f32 v77, v77, v115, v116
	v_max3_f32 v76, v76, v100, v101
	v_mfma_f32_32x32x16_bf16 v[0:15], v[80:83], v[72:75], v[0:15]
	v_max3_f32 v77, v77, v117, v118
	v_max3_f32 v76, v76, v102, v103
	v_max3_f32 v77, v77, v119, v120
	v_max3_f32 v76, v76, v104, v105
	v_max3_f32 v77, v77, v121, v122
	v_max3_f32 v76, v76, v106, v107
	v_max3_f32 v77, v77, v123, v124
	v_mfma_f32_32x32x16_bf16 v[0:15], v[84:87], v[64:67], v[0:15]
	v_max3_f32 v76, v76, v108, v109
	v_max3_f32 v77, v77, v125, v126
	v_max3_f32 v76, v76, v110, v111
	v_max3_f32 v194, v77, v127, v76
	ds_read_b64_tr_b16 v[76:77], v209 offset:0x200
	ds_read_b64_tr_b16 v[78:79], v209 offset:0xa00
	ds_read_b64_tr_b16 v[80:81], v209 offset:0x1200
	v_mfma_f32_32x32x16_bf16 v[0:15], v[92:95], v[68:71], v[0:15]
	ds_read_b64_tr_b16 v[82:83], v209 offset:0x1a00
	ds_read_b64_tr_b16 v[84:85], v209 offset:0x2200
	ds_read_b64_tr_b16 v[86:87], v209 offset:0x2a00
	ds_read_b64_tr_b16 v[92:93], v209 offset:0x3200
	ds_read_b64_tr_b16 v[94:95], v209 offset:0x3a00
	s_waitcnt lgkmcnt(0)
	v_mfma_f32_32x32x16_bf16 v[48:63], v[76:79], v[88:91], v[48:63]
	v_mov_b32_e32 v76, v194
	s_nop 1
	v_permlane32_swap_b32_e32 v194, v76
	v_max_f32_e32 v76, v76, v76
	v_max_f32_e32 v77, v194, v194
	v_max_f32_e32 v76, v77, v76
	v_sub_f32_e32 v77, v76, v226
	v_mfma_f32_32x32x16_bf16 v[48:63], v[80:83], v[72:75], v[48:63]
	v_cmp_ge_f32_e32 vcc, s31, v77
	v_max_f32_e32 v77, v226, v226
	v_max_f32_e32 v76, v77, v76
	v_sub_f32_e32 v77, v226, v76
	v_mul_f32_e32 v77, 0x3e0293ee, v77
	v_exp_f32_e32 v77, v77
	s_cmp_eq_u64 vcc, exec
	v_mfma_f32_32x32x16_bf16 v[48:63], v[84:87], v[64:67], v[48:63]
	s_cselect_b64 vcc, -1, 0
	v_cndmask_b32_e64 v210, v77, 1.0, vcc
	v_cndmask_b32_e32 v226, v76, v226, vcc
	ds_read_b64_tr_b16 v[76:77], v209 offset:0x400
	ds_read_b64_tr_b16 v[78:79], v209 offset:0xc00
	ds_read_b64_tr_b16 v[80:81], v209 offset:0x1400
	ds_read_b64_tr_b16 v[82:83], v209 offset:0x1c00
	v_mfma_f32_32x32x16_bf16 v[48:63], v[92:95], v[68:71], v[48:63]
	ds_read_b64_tr_b16 v[84:85], v209 offset:0x2400
	ds_read_b64_tr_b16 v[86:87], v209 offset:0x2c00
	ds_read_b64_tr_b16 v[92:93], v209 offset:0x3400
	ds_read_b64_tr_b16 v[94:95], v209 offset:0x3c00
	s_waitcnt lgkmcnt(0)
	v_mul_f32_e32 v208, 0xbe0293ee, v226
	v_fmamk_f32 v194, v112, 0x3e0293ee, v208
	v_fmamk_f32 v195, v113, 0x3e0293ee, v208
	v_fmamk_f32 v196, v114, 0x3e0293ee, v208
	v_fmamk_f32 v197, v115, 0x3e0293ee, v208
	v_fmamk_f32 v229, v116, 0x3e0293ee, v208
	v_fmamk_f32 v233, v117, 0x3e0293ee, v208
	v_fmamk_f32 v234, v118, 0x3e0293ee, v208
	v_fmamk_f32 v235, v119, 0x3e0293ee, v208
	v_fmamk_f32 v236, v120, 0x3e0293ee, v208
	v_fmamk_f32 v237, v121, 0x3e0293ee, v208
	v_fmamk_f32 v238, v122, 0x3e0293ee, v208
	v_fmamk_f32 v239, v123, 0x3e0293ee, v208
	v_fmamk_f32 v240, v124, 0x3e0293ee, v208
	v_fmamk_f32 v241, v125, 0x3e0293ee, v208
	v_fmamk_f32 v242, v126, 0x3e0293ee, v208
	v_fmamk_f32 v243, v127, 0x3e0293ee, v208
	v_mfma_f32_32x32x16_bf16 v[32:47], v[76:79], v[88:91], v[32:47]
	ds_read_b64_tr_b16 v[76:77], v209 offset:0x600
	ds_read_b64_tr_b16 v[78:79], v209 offset:0xe00
	v_fma_f32 v112, v96, s52, v208
	v_fma_f32 v113, v97, s52, v208
	v_fma_f32 v114, v98, s52, v208
	v_fma_f32 v115, v99, s52, v208
	v_fma_f32 v116, v100, s52, v208
	v_fma_f32 v117, v101, s52, v208
	v_pk_fma_f32 v[118:119], v[102:103], s[52:53], v[208:209] op_sel_hi:[1,0,0]
	v_pk_fma_f32 v[126:127], v[110:111], s[52:53], v[208:209] op_sel_hi:[1,0,0]
	v_mfma_f32_32x32x16_bf16 v[32:47], v[80:83], v[72:75], v[32:47]
	v_exp_f32_e32 v80, v194
	v_exp_f32_e32 v81, v195
	v_exp_f32_e32 v82, v196
	v_exp_f32_e32 v83, v197
	v_pk_fma_f32 v[124:125], v[108:109], s[52:53], v[208:209] op_sel_hi:[1,0,0]
	v_pk_fma_f32 v[122:123], v[106:107], s[52:53], v[208:209] op_sel_hi:[1,0,0]
	v_pk_fma_f32 v[120:121], v[104:105], s[52:53], v[208:209] op_sel_hi:[1,0,0]
	v_mfma_f32_32x32x16_bf16 v[32:47], v[84:87], v[64:67], v[32:47]
	v_exp_f32_e32 v84, v229
	v_exp_f32_e32 v85, v233
	v_exp_f32_e32 v86, v234
	v_exp_f32_e32 v87, v235
	v_mfma_f32_32x32x16_bf16 v[32:47], v[92:95], v[68:71], v[32:47]
	ds_read_b64_tr_b16 v[92:93], v209 offset:0x1600
	ds_read_b64_tr_b16 v[94:95], v209 offset:0x1e00
	ds_read_b64_tr_b16 v[96:97], v209 offset:0x2600
	ds_read_b64_tr_b16 v[98:99], v209 offset:0x2e00
	ds_read_b64_tr_b16 v[100:101], v209 offset:0x3600
	ds_read_b64_tr_b16 v[102:103], v209 offset:0x3e00
	s_waitcnt lgkmcnt(0)
	v_mfma_f32_32x32x16_bf16 v[16:31], v[76:79], v[88:91], v[16:31]
	v_exp_f32_e32 v88, v236
	v_exp_f32_e32 v89, v237
	v_exp_f32_e32 v90, v238
	v_exp_f32_e32 v91, v239
	v_cmp_gt_f32_e32 vcc, 1.0, v210
	v_mfma_f32_32x32x16_bf16 v[16:31], v[92:95], v[72:75], v[16:31]
	v_exp_f32_e32 v92, v240
	v_exp_f32_e32 v93, v241
	v_exp_f32_e32 v94, v242
	v_exp_f32_e32 v95, v243
	s_barrier
	v_mfma_f32_32x32x16_bf16 v[16:31], v[96:99], v[64:67], v[16:31]
	s_waitcnt vmcnt(4)
	s_waitcnt vmcnt(7)
	ds_write_b128 v212, v[162:165]
	s_waitcnt vmcnt(6)
	ds_write_b128 v213, v[166:169]
	s_waitcnt vmcnt(5)
	ds_write_b128 v214, v[170:173] offset:32768
	s_waitcnt vmcnt(4)
	ds_write_b128 v215, v[174:177] offset:32768
	v_mfma_f32_32x32x16_bf16 v[16:31], v[100:103], v[68:71], v[16:31]
	s_cbranch_vccz .Lgqa_slow_883
	v_pk_mul_f32 v[14:15], v[14:15], v[210:211] op_sel_hi:[1,0]
	v_pk_mul_f32 v[12:13], v[12:13], v[210:211] op_sel_hi:[1,0]
	v_pk_mul_f32 v[10:11], v[10:11], v[210:211] op_sel_hi:[1,0]
	v_pk_mul_f32 v[8:9], v[8:9], v[210:211] op_sel_hi:[1,0]
	v_pk_mul_f32 v[6:7], v[6:7], v[210:211] op_sel_hi:[1,0]
	v_pk_mul_f32 v[4:5], v[4:5], v[210:211] op_sel_hi:[1,0]
	v_pk_mul_f32 v[2:3], v[2:3], v[210:211] op_sel_hi:[1,0]
	v_pk_mul_f32 v[0:1], v[0:1], v[210:211] op_sel_hi:[1,0]
	v_pk_mul_f32 v[62:63], v[62:63], v[210:211] op_sel_hi:[1,0]
	v_pk_mul_f32 v[60:61], v[60:61], v[210:211] op_sel_hi:[1,0]
	v_pk_mul_f32 v[58:59], v[58:59], v[210:211] op_sel_hi:[1,0]
	v_pk_mul_f32 v[56:57], v[56:57], v[210:211] op_sel_hi:[1,0]
	v_pk_mul_f32 v[54:55], v[54:55], v[210:211] op_sel_hi:[1,0]
	v_pk_mul_f32 v[52:53], v[52:53], v[210:211] op_sel_hi:[1,0]
	v_pk_mul_f32 v[50:51], v[50:51], v[210:211] op_sel_hi:[1,0]
	v_pk_mul_f32 v[48:49], v[48:49], v[210:211] op_sel_hi:[1,0]
	v_pk_mul_f32 v[46:47], v[210:211], v[46:47] op_sel_hi:[0,1]
	v_pk_mul_f32 v[44:45], v[210:211], v[44:45] op_sel_hi:[0,1]
	v_pk_mul_f32 v[42:43], v[210:211], v[42:43] op_sel_hi:[0,1]
	v_pk_mul_f32 v[40:41], v[210:211], v[40:41] op_sel_hi:[0,1]
	v_pk_mul_f32 v[38:39], v[210:211], v[38:39] op_sel_hi:[0,1]
	v_pk_mul_f32 v[36:37], v[210:211], v[36:37] op_sel_hi:[0,1]
	v_pk_mul_f32 v[34:35], v[210:211], v[34:35] op_sel_hi:[0,1]
	v_pk_mul_f32 v[32:33], v[210:211], v[32:33] op_sel_hi:[0,1]
	v_pk_mul_f32 v[30:31], v[210:211], v[30:31] op_sel_hi:[0,1]
	v_pk_mul_f32 v[28:29], v[210:211], v[28:29] op_sel_hi:[0,1]
	v_pk_mul_f32 v[26:27], v[210:211], v[26:27] op_sel_hi:[0,1]
	v_pk_mul_f32 v[24:25], v[210:211], v[24:25] op_sel_hi:[0,1]
	v_pk_mul_f32 v[22:23], v[210:211], v[22:23] op_sel_hi:[0,1]
	v_pk_mul_f32 v[20:21], v[210:211], v[20:21] op_sel_hi:[0,1]
	v_pk_mul_f32 v[18:19], v[210:211], v[18:19] op_sel_hi:[0,1]
	v_pk_mul_f32 v[16:17], v[210:211], v[16:17] op_sel_hi:[0,1]
.Lgqa_slow_883:
	s_waitcnt lgkmcnt(0)
	s_barrier
	ds_read_b128 v[64:67], v216 offset:32768
	ds_read_b128 v[68:71], v216 offset:40960
	ds_read_b128 v[162:165], v218 offset:32768
	ds_read_b128 v[166:169], v218 offset:40960
	v_exp_f32_e32 v112, v112
	v_exp_f32_e32 v113, v113
	s_waitcnt lgkmcnt(3)
	v_mfma_f32_32x32x16_bf16 v[96:111], v[64:67], v[138:141], 0
	v_exp_f32_e32 v114, v114
	v_exp_f32_e32 v115, v115
	v_exp_f32_e32 v116, v116
	v_exp_f32_e32 v117, v117
	v_exp_f32_e32 v118, v118
	v_exp_f32_e32 v119, v119
	s_waitcnt lgkmcnt(2)
	v_mfma_f32_32x32x16_bf16 v[64:79], v[68:71], v[138:141], 0
	s_waitcnt lgkmcnt(1)
	v_mfma_f32_32x32x16_bf16 v[96:111], v[162:165], v[154:157], v[96:111]
	s_waitcnt lgkmcnt(0)
	v_mfma_f32_32x32x16_bf16 v[64:79], v[166:169], v[154:157], v[64:79]
	ds_read_b128 v[162:165], v219 offset:32768
	ds_read_b128 v[166:169], v219 offset:40960
	s_waitcnt lgkmcnt(1)
	v_mfma_f32_32x32x16_bf16 v[96:111], v[162:165], v[158:161], v[96:111]
	s_waitcnt lgkmcnt(0)
	v_mfma_f32_32x32x16_bf16 v[64:79], v[166:169], v[158:161], v[64:79]
	ds_read_b128 v[162:165], v220 offset:32768
	ds_read_b128 v[166:169], v220 offset:40960
	s_waitcnt lgkmcnt(1)
	v_mfma_f32_32x32x16_bf16 v[96:111], v[162:165], v[150:153], v[96:111]
	s_waitcnt lgkmcnt(0)
	v_mfma_f32_32x32x16_bf16 v[64:79], v[166:169], v[150:153], v[64:79]
	ds_read_b128 v[162:165], v221 offset:32768
	ds_read_b128 v[166:169], v221 offset:40960
	s_waitcnt lgkmcnt(1)
	v_mfma_f32_32x32x16_bf16 v[96:111], v[162:165], v[146:149], v[96:111]
	s_waitcnt lgkmcnt(0)
	v_mfma_f32_32x32x16_bf16 v[64:79], v[166:169], v[146:149], v[64:79]
	ds_read_b128 v[162:165], v222 offset:32768
	ds_read_b128 v[166:169], v222 offset:40960
	s_waitcnt lgkmcnt(1)
	v_mfma_f32_32x32x16_bf16 v[96:111], v[162:165], v[142:145], v[96:111]
	s_waitcnt lgkmcnt(0)
	v_mfma_f32_32x32x16_bf16 v[64:79], v[166:169], v[142:145], v[64:79]
	ds_read_b128 v[162:165], v224 offset:32768
	ds_read_b128 v[166:169], v224 offset:40960
	s_waitcnt lgkmcnt(1)
	v_mfma_f32_32x32x16_bf16 v[96:111], v[162:165], v[134:137], v[96:111]
	s_waitcnt lgkmcnt(0)
	v_mfma_f32_32x32x16_bf16 v[64:79], v[166:169], v[134:137], v[64:79]
	ds_read_b128 v[162:165], v223 offset:32768
	ds_read_b128 v[166:169], v223 offset:40960
	s_waitcnt lgkmcnt(1)
	v_mfma_f32_32x32x16_bf16 v[96:111], v[162:165], v[130:133], v[96:111]
	v_exp_f32_e32 v162, v120
	v_exp_f32_e32 v163, v121
	v_exp_f32_e32 v164, v122
	v_exp_f32_e32 v165, v123
	v_add_f32_e32 v120, v80, v81
	v_add_f32_e32 v121, v88, v89
	v_add_f32_e32 v122, v112, v113
	s_waitcnt lgkmcnt(0)
	v_mfma_f32_32x32x16_bf16 v[64:79], v[166:169], v[130:133], v[64:79]
	v_exp_f32_e32 v166, v124
	v_exp_f32_e32 v167, v125
	v_add_f32_e32 v123, v162, v163
	v_exp_f32_e32 v168, v126
	v_add_f32_e32 v120, v82, v120
	v_add_f32_e32 v121, v90, v121
	v_add_f32_e32 v122, v114, v122
	v_add_f32_e32 v123, v164, v123
	v_exp_f32_e32 v169, v127
	v_add_f32_e32 v120, v83, v120
	v_add_f32_e32 v121, v91, v121
	v_add_f32_e32 v122, v115, v122
	v_add_f32_e32 v123, v165, v123
	v_add_f32_e32 v120, v84, v120
	v_add_f32_e32 v121, v92, v121
	v_add_f32_e32 v122, v116, v122
	v_add_f32_e32 v123, v166, v123
	v_add_f32_e32 v120, v85, v120
	v_add_f32_e32 v121, v93, v121
	v_add_f32_e32 v122, v117, v122
	v_add_f32_e32 v123, v167, v123
	v_add_f32_e32 v120, v86, v120
	v_add_f32_e32 v121, v94, v121
	v_add_f32_e32 v122, v118, v122
	v_add_f32_e32 v123, v168, v123
	v_add_f32_e32 v120, v87, v120
	v_add_f32_e32 v121, v95, v121
	v_add_f32_e32 v122, v119, v122
	v_add_f32_e32 v123, v169, v123
	v_add_f32_e32 v120, v121, v120
	v_add_f32_e32 v121, v123, v122
	v_add_f32_e32 v229, v120, v121
	v_mov_b32_e32 v233, v229
	s_nop 1
	v_permlane32_swap_b32_e32 v229, v233
	v_cvt_pk_bf16_f32 v124, v80, v81
	v_cvt_pk_bf16_f32 v125, v82, v83
	v_cvt_pk_bf16_f32 v126, v84, v85
	v_cvt_pk_bf16_f32 v127, v86, v87
	v_cvt_pk_bf16_f32 v120, v88, v89
	v_cvt_pk_bf16_f32 v121, v90, v91
	v_cvt_pk_bf16_f32 v122, v92, v93
	v_cvt_pk_bf16_f32 v123, v94, v95
	v_cvt_pk_bf16_f32 v112, v112, v113
	v_cvt_pk_bf16_f32 v113, v114, v115
	v_cvt_pk_bf16_f32 v114, v116, v117
	v_cvt_pk_bf16_f32 v115, v118, v119
	v_cvt_pk_bf16_f32 v116, v162, v163
	v_cvt_pk_bf16_f32 v117, v164, v165
	v_cvt_pk_bf16_f32 v118, v166, v167
	v_cvt_pk_bf16_f32 v119, v168, v169
	s_nop 0
	v_permlane32_swap_b32_e32 v124, v126
	v_permlane32_swap_b32_e32 v125, v127
	v_permlane32_swap_b32_e32 v120, v122
	v_permlane32_swap_b32_e32 v121, v123
	v_permlane32_swap_b32_e32 v112, v114
	v_permlane32_swap_b32_e32 v113, v115
	v_permlane32_swap_b32_e32 v116, v118
	v_permlane32_swap_b32_e32 v117, v119
	s_min_i32 s2, s39, s14
	s_mul_i32 s2, s2, s62
	s_lshl_b32 s72, s2, 6
	s_lshl_b64 s[2:3], s[72:73], 1
	s_add_u32 s12, s10, s2
	s_addc_u32 s13, s11, s3
	s_add_u32 s2, s8, s2
	s_addc_u32 s3, s9, s3
	v_lshl_add_u64 v[80:81], s[12:13], 0, v[128:129]
	v_lshl_add_u64 v[82:83], s[12:13], 0, v[198:199]
	global_load_dwordx4 v[162:165], v[80:81], off
	global_load_dwordx4 v[166:169], v[82:83], off
	v_lshl_add_u64 v[80:81], s[2:3], 0, v[128:129]
	v_lshl_add_u64 v[82:83], s[2:3], 0, v[198:199]
	global_load_dwordx4 v[170:173], v[80:81], off
	global_load_dwordx4 v[174:177], v[82:83], off
	ds_read_b64_tr_b16 v[80:81], v211 offset:0
	ds_read_b64_tr_b16 v[82:83], v211 offset:0x800
	ds_read_b64_tr_b16 v[84:85], v211 offset:0x1000
	ds_read_b64_tr_b16 v[86:87], v211 offset:0x1800
	ds_read_b64_tr_b16 v[88:89], v211 offset:0x2000
	ds_read_b64_tr_b16 v[90:91], v211 offset:0x2800
	ds_read_b64_tr_b16 v[92:93], v211 offset:0x3000
	ds_read_b64_tr_b16 v[94:95], v211 offset:0x3800
	s_waitcnt lgkmcnt(0)
	s_nop 0
	v_mfma_f32_32x32x16_bf16 v[0:15], v[80:83], v[124:127], v[0:15]
	v_max_f32_e32 v80, v65, v65
	v_max_f32_e32 v81, v64, v64
	v_max_f32_e32 v80, v81, v80
	v_max3_f32 v81, v96, v97, v98
	v_max3_f32 v80, v80, v66, v67
	v_max3_f32 v81, v81, v99, v100
	v_max3_f32 v80, v80, v68, v69
	v_mfma_f32_32x32x16_bf16 v[0:15], v[84:87], v[120:123], v[0:15]
	v_max3_f32 v81, v81, v101, v102
	v_max3_f32 v80, v80, v70, v71
	v_max3_f32 v81, v81, v103, v104
	v_max3_f32 v80, v80, v72, v73
	v_max3_f32 v81, v81, v105, v106
	v_max3_f32 v80, v80, v74, v75
	v_max3_f32 v81, v81, v107, v108
	v_mfma_f32_32x32x16_bf16 v[0:15], v[88:91], v[112:115], v[0:15]
	v_max3_f32 v80, v80, v76, v77
	v_max3_f32 v81, v81, v109, v110
	v_max3_f32 v80, v80, v78, v79
	v_max3_f32 v194, v81, v111, v80
	ds_read_b64_tr_b16 v[80:81], v211 offset:0x200
	ds_read_b64_tr_b16 v[82:83], v211 offset:0xa00
	ds_read_b64_tr_b16 v[84:85], v211 offset:0x1200
	v_mfma_f32_32x32x16_bf16 v[0:15], v[92:95], v[116:119], v[0:15]
	ds_read_b64_tr_b16 v[86:87], v211 offset:0x1a00
	ds_read_b64_tr_b16 v[88:89], v211 offset:0x2200
	ds_read_b64_tr_b16 v[90:91], v211 offset:0x2a00
	ds_read_b64_tr_b16 v[92:93], v211 offset:0x3200
	ds_read_b64_tr_b16 v[94:95], v211 offset:0x3a00
	s_waitcnt lgkmcnt(0)
	v_mfma_f32_32x32x16_bf16 v[48:63], v[80:83], v[124:127], v[48:63]
	v_mov_b32_e32 v80, v194
	s_nop 1
	v_permlane32_swap_b32_e32 v194, v80
	v_max_f32_e32 v80, v80, v80
	v_max_f32_e32 v81, v194, v194
	v_max_f32_e32 v80, v81, v80
	v_sub_f32_e32 v81, v80, v226
	v_mfma_f32_32x32x16_bf16 v[48:63], v[84:87], v[120:123], v[48:63]
	v_cmp_ge_f32_e32 vcc, s31, v81
	v_max_f32_e32 v81, v226, v226
	v_max_f32_e32 v80, v81, v80
	v_sub_f32_e32 v81, v226, v80
	v_mul_f32_e32 v81, 0x3e0293ee, v81
	v_exp_f32_e32 v81, v81
	s_cmp_eq_u64 vcc, exec
	v_mfma_f32_32x32x16_bf16 v[48:63], v[88:91], v[112:115], v[48:63]
	s_cselect_b64 vcc, -1, 0
	v_cndmask_b32_e64 v208, v81, 1.0, vcc
	v_cndmask_b32_e32 v226, v80, v226, vcc
	ds_read_b64_tr_b16 v[80:81], v211 offset:0x400
	ds_read_b64_tr_b16 v[82:83], v211 offset:0xc00
	ds_read_b64_tr_b16 v[84:85], v211 offset:0x1400
	ds_read_b64_tr_b16 v[86:87], v211 offset:0x1c00
	v_mfma_f32_32x32x16_bf16 v[48:63], v[92:95], v[116:119], v[48:63]
	ds_read_b64_tr_b16 v[88:89], v211 offset:0x2400
	ds_read_b64_tr_b16 v[90:91], v211 offset:0x2c00
	ds_read_b64_tr_b16 v[92:93], v211 offset:0x3400
	ds_read_b64_tr_b16 v[94:95], v211 offset:0x3c00
	s_waitcnt lgkmcnt(0)
	v_mul_f32_e32 v234, 0xbe0293ee, v226
	v_fmamk_f32 v96, v96, 0x3e0293ee, v234
	v_fmamk_f32 v97, v97, 0x3e0293ee, v234
	v_fmamk_f32 v98, v98, 0x3e0293ee, v234
	v_fmamk_f32 v99, v99, 0x3e0293ee, v234
	v_fmamk_f32 v100, v100, 0x3e0293ee, v234
	v_fmamk_f32 v101, v101, 0x3e0293ee, v234
	v_fmamk_f32 v102, v102, 0x3e0293ee, v234
	v_fmamk_f32 v103, v103, 0x3e0293ee, v234
	v_fmamk_f32 v104, v104, 0x3e0293ee, v234
	v_fmamk_f32 v105, v105, 0x3e0293ee, v234
	v_fmamk_f32 v106, v106, 0x3e0293ee, v234
	v_fmamk_f32 v107, v107, 0x3e0293ee, v234
	v_fmamk_f32 v108, v108, 0x3e0293ee, v234
	v_fmamk_f32 v109, v109, 0x3e0293ee, v234
	v_fmamk_f32 v110, v110, 0x3e0293ee, v234
	v_fmamk_f32 v111, v111, 0x3e0293ee, v234
	v_mfma_f32_32x32x16_bf16 v[32:47], v[80:83], v[124:127], v[32:47]
	v_fma_f32 v80, v64, s52, v234
	v_fma_f32 v81, v65, s52, v234
	v_exp_f32_e32 v64, v96
	v_exp_f32_e32 v65, v97
	v_pk_fma_f32 v[82:83], v[66:67], s[52:53], v[234:235] op_sel_hi:[1,0,0]
	v_exp_f32_e32 v66, v98
	v_exp_f32_e32 v67, v99
	v_mfma_f32_32x32x16_bf16 v[32:47], v[84:87], v[120:123], v[32:47]
	v_fma_f32 v84, v68, s52, v234
	v_fma_f32 v85, v69, s52, v234
	v_exp_f32_e32 v68, v100
	v_exp_f32_e32 v69, v101
	v_pk_fma_f32 v[86:87], v[70:71], s[52:53], v[234:235] op_sel_hi:[1,0,0]
	v_exp_f32_e32 v70, v102
	v_exp_f32_e32 v71, v103
	v_mfma_f32_32x32x16_bf16 v[32:47], v[88:91], v[112:115], v[32:47]
	v_fma_f32 v88, v72, s52, v234
	v_fma_f32 v89, v73, s52, v234
	ds_read_b64_tr_b16 v[72:73], v211 offset:0x600
	v_fma_f32 v90, v74, s52, v234
	v_fma_f32 v91, v75, s52, v234
	ds_read_b64_tr_b16 v[74:75], v211 offset:0xe00
	v_mfma_f32_32x32x16_bf16 v[32:47], v[92:95], v[116:119], v[32:47]
	v_fma_f32 v92, v76, s52, v234
	v_fma_f32 v93, v77, s52, v234
	ds_read_b64_tr_b16 v[76:77], v211 offset:0x1600
	v_fma_f32 v94, v78, s52, v234
	v_fma_f32 v95, v79, s52, v234
	ds_read_b64_tr_b16 v[78:79], v211 offset:0x1e00
	ds_read_b64_tr_b16 v[96:97], v211 offset:0x2600
	ds_read_b64_tr_b16 v[98:99], v211 offset:0x2e00
	ds_read_b64_tr_b16 v[100:101], v211 offset:0x3600
	ds_read_b64_tr_b16 v[102:103], v211 offset:0x3e00
	s_waitcnt lgkmcnt(0)
	v_mfma_f32_32x32x16_bf16 v[16:31], v[72:75], v[124:127], v[16:31]
	v_exp_f32_e32 v72, v104
	v_exp_f32_e32 v73, v105
	v_exp_f32_e32 v74, v106
	v_exp_f32_e32 v75, v107
	v_cmp_gt_f32_e32 vcc, 1.0, v208
	v_mfma_f32_32x32x16_bf16 v[16:31], v[76:79], v[120:123], v[16:31]
	v_exp_f32_e32 v76, v108
	v_exp_f32_e32 v77, v109
	v_exp_f32_e32 v78, v110
	v_exp_f32_e32 v79, v111
	s_barrier
	v_mfma_f32_32x32x16_bf16 v[16:31], v[96:99], v[112:115], v[16:31]
	s_waitcnt vmcnt(4)
	s_waitcnt vmcnt(7)
	ds_write_b128 v212, v[178:181] offset:16384
	s_waitcnt vmcnt(6)
	ds_write_b128 v213, v[182:185] offset:16384
	s_waitcnt vmcnt(5)
	ds_write_b128 v214, v[186:189] offset:49152
	s_waitcnt vmcnt(4)
	ds_write_b128 v215, v[190:193] offset:49152
	v_mfma_f32_32x32x16_bf16 v[16:31], v[100:103], v[116:119], v[16:31]
	s_cbranch_vccz .Lgqa_slow_885
	v_pk_mul_f32 v[14:15], v[14:15], v[208:209] op_sel_hi:[1,0]
	v_pk_mul_f32 v[12:13], v[12:13], v[208:209] op_sel_hi:[1,0]
	v_pk_mul_f32 v[10:11], v[10:11], v[208:209] op_sel_hi:[1,0]
	v_pk_mul_f32 v[8:9], v[8:9], v[208:209] op_sel_hi:[1,0]
	v_pk_mul_f32 v[6:7], v[6:7], v[208:209] op_sel_hi:[1,0]
	v_pk_mul_f32 v[4:5], v[4:5], v[208:209] op_sel_hi:[1,0]
	v_pk_mul_f32 v[2:3], v[2:3], v[208:209] op_sel_hi:[1,0]
	v_pk_mul_f32 v[0:1], v[0:1], v[208:209] op_sel_hi:[1,0]
	v_pk_mul_f32 v[62:63], v[62:63], v[208:209] op_sel_hi:[1,0]
	v_pk_mul_f32 v[60:61], v[60:61], v[208:209] op_sel_hi:[1,0]
	v_pk_mul_f32 v[58:59], v[58:59], v[208:209] op_sel_hi:[1,0]
	v_pk_mul_f32 v[56:57], v[56:57], v[208:209] op_sel_hi:[1,0]
	v_pk_mul_f32 v[54:55], v[54:55], v[208:209] op_sel_hi:[1,0]
	v_pk_mul_f32 v[52:53], v[52:53], v[208:209] op_sel_hi:[1,0]
	v_pk_mul_f32 v[50:51], v[50:51], v[208:209] op_sel_hi:[1,0]
	v_pk_mul_f32 v[48:49], v[48:49], v[208:209] op_sel_hi:[1,0]
	v_pk_mul_f32 v[46:47], v[208:209], v[46:47] op_sel_hi:[0,1]
	v_pk_mul_f32 v[44:45], v[208:209], v[44:45] op_sel_hi:[0,1]
	v_pk_mul_f32 v[42:43], v[208:209], v[42:43] op_sel_hi:[0,1]
	v_pk_mul_f32 v[40:41], v[208:209], v[40:41] op_sel_hi:[0,1]
	v_pk_mul_f32 v[38:39], v[208:209], v[38:39] op_sel_hi:[0,1]
	v_pk_mul_f32 v[36:37], v[208:209], v[36:37] op_sel_hi:[0,1]
	v_pk_mul_f32 v[34:35], v[208:209], v[34:35] op_sel_hi:[0,1]
	v_pk_mul_f32 v[32:33], v[208:209], v[32:33] op_sel_hi:[0,1]
	v_pk_mul_f32 v[30:31], v[208:209], v[30:31] op_sel_hi:[0,1]
	v_pk_mul_f32 v[28:29], v[208:209], v[28:29] op_sel_hi:[0,1]
	v_pk_mul_f32 v[26:27], v[208:209], v[26:27] op_sel_hi:[0,1]
	v_pk_mul_f32 v[24:25], v[208:209], v[24:25] op_sel_hi:[0,1]
	v_pk_mul_f32 v[22:23], v[208:209], v[22:23] op_sel_hi:[0,1]
	v_pk_mul_f32 v[20:21], v[208:209], v[20:21] op_sel_hi:[0,1]
	v_pk_mul_f32 v[18:19], v[208:209], v[18:19] op_sel_hi:[0,1]
	v_pk_mul_f32 v[16:17], v[208:209], v[16:17] op_sel_hi:[0,1]
.Lgqa_slow_885:
	v_add_f32_e32 v96, v227, v228
	v_fmac_f32_e32 v96, v217, v225
	v_add_f32_e32 v217, v229, v233
	s_add_i32 s2, s39, 2
	s_add_i32 s3, s39, -1
	v_fmac_f32_e32 v217, v96, v210
	v_lshl_add_u64 v[200:201], v[200:201], 0, s[6:7]
	v_lshl_add_u64 v[202:203], v[202:203], 0, s[6:7]
	v_lshl_add_u64 v[204:205], v[204:205], 0, s[6:7]
	s_cmp_ge_u32 s3, s14
	v_lshl_add_u64 v[206:207], v[206:207], 0, s[6:7]
	s_waitcnt lgkmcnt(0)
	s_barrier
	s_cbranch_scc1 .Lgqa_slow_887
	s_mov_b32 s39, s2
	v_mov_b32_e32 v225, v208
	s_branch .Lgqa_slow_881
